# baseline (speedup 1.0000x reference)
_Z16sum_layer_kernelPKfS0_Pf:
	s_load_dwordx4 s[4:7], s[0:1], 0x0
	s_load_dwordx2 s[8:9], s[0:1], 0x10
	s_and_b32 s40, s2, 7
	s_lshl_b32 s40, s40, 6
	s_lshr_b32 s2, s2, 3
	s_or_b32 s2, s2, s40
	v_and_b32_e32 v40, 31, v0
	v_bfe_u32 v41, v0, 5, 1
	v_lshrrev_b32_e32 v42, 6, v0
	v_and_b32_e32 v43, 7, v0
	v_bfe_u32 v44, v0, 3, 3
	v_and_b32_e32 v45, 63, v0
	s_lshl_b32 s3, s2, 12
	s_lshl_b32 s19, s2, 7
	v_lshlrev_b32_e32 v1, 11, v41
	v_lshl_or_b32 v1, v40, 2, v1
	v_lshlrev_b32_e32 v46, 4, v43
	v_lshl_add_u32 v35, v44, 16, v46
	v_lshl_add_u32 v35, v42, 21, v35
	v_add_u32_e32 v35, s19, v35
	v_lshlrev_b32_e32 v36, 2, v40
	v_lshl_add_u32 v36, v41, 18, v36
	v_lshl_add_u32 v36, v42, 21, v36
	v_add_u32_e32 v36, s19, v36
	v_mul_u32_u24_e32 v37, 0x1200, v42
	v_mul_u32_u24_e32 v38, 0x90, v44
	v_add3_u32 v38, v37, v38, v46
	v_mul_u32_u24_e32 v39, 0x90, v40
	v_lshlrev_b32_e32 v47, 6, v41
	v_add3_u32 v39, v37, v39, v47
	v_lshrrev_b32_e32 v46, 1, v44
	v_xor_b32_e32 v46, v43, v46
	v_lshlrev_b32_e32 v46, 4, v46
	v_lshl_add_u32 v35, v44, 16, v46
	v_lshl_add_u32 v35, v42, 21, v35
	v_add_u32_e32 v35, s19, v35
	v_xor_b32_e32 v86, 64, v35
	v_readfirstlane_b32 s23, v42
	v_bfe_u32 v47, v40, 1, 3
	v_lshlrev_b32_e32 v39, 2, v41
	v_xor_b32_e32 v39, v39, v47
	s_lshl_b32 s23, s23, 12
	v_lshlrev_b32_e32 v39, 4, v39
	v_lshl_add_u32 v39, v40, 7, v39
	v_lshl_add_u32 v39, v42, 12, v39
	s_mov_b32 m0, s23
	v_xor_b32_e32 v81, 16, v39
	v_xor_b32_e32 v82, 32, v39
	v_xor_b32_e32 v83, 48, v39
	v_cmp_gt_u32_e32 vcc, 32, v45
	v_mov_b32_e32 v34, 0xc1600000
	v_mov_b32_e32 v84, 0x3fb8aa3b
	v_mov_b32_e32 v85, 0x3f317218
	s_mov_b32 s16, 0x3fb8aa3b
	s_mov_b32 s17, 0x3f317218
	s_mov_b32 s20, 0x7fc00
	s_mov_b32 s21, 0xff800
	s_mov_b32 s22, 0x17f400
	s_lshl_b32 s24, 1, 16
	s_lshl_b32 s25, 2, 16
	s_lshl_b32 s26, 3, 16
	s_lshl_b32 s27, 8, 16
	s_lshl_b32 s28, 9, 16
	s_lshl_b32 s29, 10, 16
	s_lshl_b32 s30, 11, 16
	s_lshl_b32 s31, 16, 16
	s_lshl_b32 s32, 17, 16
	s_lshl_b32 s33, 18, 16
	s_lshl_b32 s34, 19, 16
	s_lshl_b32 s35, 24, 16
	s_lshl_b32 s36, 25, 16
	s_lshl_b32 s37, 26, 16
	s_lshl_b32 s38, 27, 16
	s_mov_b32 s14, 0x200000
	s_mov_b32 s15, 0x20000
	s_waitcnt lgkmcnt(0)
	s_mov_b32 s12, s6
	s_and_b32 s13, s7, 0xffff
	s_and_b32 s5, s5, 0xffff
	s_mov_b32 s6, 0x800000
	s_mov_b32 s7, s15
	s_and_b32 s9, s9, 0xffff
	s_mov_b32 s10, s6
	s_mov_b32 s11, s15
	buffer_load_dword v18, v1, s[12:15], s3 offen nt
	buffer_load_dword v19, v1, s[12:15], s3 offen offset:128 nt
	buffer_load_dword v20, v1, s[12:15], s3 offen offset:256 nt
	buffer_load_dword v21, v1, s[12:15], s3 offen offset:384 nt
	buffer_load_dword v22, v1, s[12:15], s3 offen offset:512 nt
	buffer_load_dword v23, v1, s[12:15], s3 offen offset:640 nt
	buffer_load_dword v24, v1, s[12:15], s3 offen offset:768 nt
	buffer_load_dword v25, v1, s[12:15], s3 offen offset:896 nt
	buffer_load_dword v26, v1, s[12:15], s3 offen offset:1024 nt
	buffer_load_dword v27, v1, s[12:15], s3 offen offset:1152 nt
	buffer_load_dword v28, v1, s[12:15], s3 offen offset:1280 nt
	buffer_load_dword v29, v1, s[12:15], s3 offen offset:1408 nt
	buffer_load_dword v30, v1, s[12:15], s3 offen offset:1536 nt
	buffer_load_dword v31, v1, s[12:15], s3 offen offset:1664 nt
	buffer_load_dword v32, v1, s[12:15], s3 offen offset:1792 nt
	buffer_load_dword v33, v1, s[12:15], s3 offen offset:1920 nt
	buffer_load_dwordx4 v35, s[4:7], 0 offen nt lds
	buffer_load_dwordx4 v86, s[4:7], s20 offen offset:1024 nt lds
	buffer_load_dwordx4 v35, s[4:7], s21 offen offset:2048 nt lds
	buffer_load_dwordx4 v86, s[4:7], s22 offen offset:3072 nt lds
	s_waitcnt vmcnt(4)
	v_max3_f32 v48, v18, v19, v20
	v_max3_f32 v50, v21, v22, v23
	v_max3_f32 v48, v48, v24, v25
	v_max3_f32 v50, v50, v26, v27
	v_max3_f32 v48, v48, v28, v29
	v_max3_f32 v50, v50, v30, v31
	v_max3_f32 v48, v48, v32, v33
	v_max_f32_e32 v48, v48, v50
	v_mov_b32_e32 v50, v48
	s_nop 1
	v_permlane32_swap_b32_e32 v48, v50
	v_max_f32_e32 v48, v48, v50
	v_fmamk_f32 v48, v48, 0x3fb8aa3b, v34
	v_pk_fma_f32 v[18:19], v[18:19], v[84:85], v[48:49] op_sel_hi:[1,0,0] neg_lo:[0,0,1] neg_hi:[0,0,1]
	v_exp_f32_e32 v18, v18
	v_exp_f32_e32 v19, v19
	v_pk_fma_f32 v[20:21], v[20:21], v[84:85], v[48:49] op_sel_hi:[1,0,0] neg_lo:[0,0,1] neg_hi:[0,0,1]
	v_exp_f32_e32 v20, v20
	v_exp_f32_e32 v21, v21
	v_pk_fma_f32 v[22:23], v[22:23], v[84:85], v[48:49] op_sel_hi:[1,0,0] neg_lo:[0,0,1] neg_hi:[0,0,1]
	v_exp_f32_e32 v22, v22
	v_exp_f32_e32 v23, v23
	v_pk_fma_f32 v[24:25], v[24:25], v[84:85], v[48:49] op_sel_hi:[1,0,0] neg_lo:[0,0,1] neg_hi:[0,0,1]
	v_exp_f32_e32 v24, v24
	v_exp_f32_e32 v25, v25
	v_pk_fma_f32 v[26:27], v[26:27], v[84:85], v[48:49] op_sel_hi:[1,0,0] neg_lo:[0,0,1] neg_hi:[0,0,1]
	v_exp_f32_e32 v26, v26
	v_exp_f32_e32 v27, v27
	v_pk_fma_f32 v[28:29], v[28:29], v[84:85], v[48:49] op_sel_hi:[1,0,0] neg_lo:[0,0,1] neg_hi:[0,0,1]
	v_exp_f32_e32 v28, v28
	v_exp_f32_e32 v29, v29
	v_pk_fma_f32 v[30:31], v[30:31], v[84:85], v[48:49] op_sel_hi:[1,0,0] neg_lo:[0,0,1] neg_hi:[0,0,1]
	v_exp_f32_e32 v30, v30
	v_exp_f32_e32 v31, v31
	v_pk_fma_f32 v[32:33], v[32:33], v[84:85], v[48:49] op_sel_hi:[1,0,0] neg_lo:[0,0,1] neg_hi:[0,0,1]
	v_exp_f32_e32 v32, v32
	v_exp_f32_e32 v33, v33
	v_pk_add_f32 v[56:57], v[18:19], v[20:21]
	v_pk_add_f32 v[58:59], v[22:23], v[24:25]
	v_pk_add_f32 v[60:61], v[26:27], v[28:29]
	v_pk_add_f32 v[62:63], v[30:31], v[32:33]
	v_pk_add_f32 v[56:57], v[56:57], v[58:59]
	v_pk_add_f32 v[60:61], v[60:61], v[62:63]
	v_pk_add_f32 v[56:57], v[56:57], v[60:61]
	v_add_f32_e32 v50, v56, v57
	v_mov_b32_e32 v51, v50
	s_nop 1
	v_permlane32_swap_b32_e32 v50, v51
	v_add_f32_e32 v50, v50, v51
	v_log_f32_e32 v50, v50
	v_cvt_pk_f16_f32 v40, v18, v19
	v_cvt_pk_f16_f32 v41, v20, v21
	v_cvt_pk_f16_f32 v42, v22, v23
	v_cvt_pk_f16_f32 v43, v24, v25
	v_cvt_pk_f16_f32 v44, v26, v27
	v_cvt_pk_f16_f32 v45, v28, v29
	v_cvt_pk_f16_f32 v46, v30, v31
	v_cvt_pk_f16_f32 v47, v32, v33
	v_add_f32_e32 v50, 0x41600000, v50
	v_mul_f32_e32 v50, 0xbf317218, v50
	v_cndmask_b32_e64 v51, v50, 1.0, vcc
	s_waitcnt vmcnt(0)
	ds_read_b128 v[2:5], v39
	ds_read_b128 v[6:9], v81
	ds_read_b128 v[10:13], v82
	ds_read_b128 v[14:17], v83
	s_waitcnt lgkmcnt(2)
	v_max3_f32 v52, v2, v3, v4
	v_max3_f32 v53, v5, v6, v7
	v_max_f32_e32 v52, v52, v8
	v_max_f32_e32 v53, v53, v9
	s_waitcnt lgkmcnt(0)
	v_max3_f32 v52, v52, v10, v11
	v_max3_f32 v53, v53, v12, v13
	v_max3_f32 v52, v52, v14, v15
	v_max3_f32 v53, v53, v16, v17
	v_max_f32_e32 v52, v52, v53
	v_mov_b32_e32 v53, v52
	s_nop 1
	v_permlane32_swap_b32_e32 v52, v53
	v_max_f32_e32 v52, v52, v53
	v_cndmask_b32_e32 v54, 1.0, v52, vcc
	v_fmamk_f32 v48, v52, 0x3fb8aa3b, v34
	v_pk_fma_f32 v[2:3], v[2:3], v[84:85], v[48:49] op_sel_hi:[1,0,0] neg_lo:[0,0,1] neg_hi:[0,0,1]
	v_mfma_f32_32x32x2_f32 v[64:79], v54, v51, 0
	v_exp_f32_e32 v2, v2
	v_exp_f32_e32 v3, v3
	v_pk_fma_f32 v[4:5], v[4:5], v[84:85], v[48:49] op_sel_hi:[1,0,0] neg_lo:[0,0,1] neg_hi:[0,0,1]
	v_exp_f32_e32 v4, v4
	v_exp_f32_e32 v5, v5
	v_pk_fma_f32 v[6:7], v[6:7], v[84:85], v[48:49] op_sel_hi:[1,0,0] neg_lo:[0,0,1] neg_hi:[0,0,1]
	v_exp_f32_e32 v6, v6
	v_exp_f32_e32 v7, v7
	v_pk_fma_f32 v[8:9], v[8:9], v[84:85], v[48:49] op_sel_hi:[1,0,0] neg_lo:[0,0,1] neg_hi:[0,0,1]
	v_exp_f32_e32 v8, v8
	v_exp_f32_e32 v9, v9
	v_pk_fma_f32 v[10:11], v[10:11], v[84:85], v[48:49] op_sel_hi:[1,0,0] neg_lo:[0,0,1] neg_hi:[0,0,1]
	v_exp_f32_e32 v10, v10
	v_cvt_pk_f16_f32 v56, v2, v3
	v_cvt_pk_f16_f32 v57, v4, v5
	v_cvt_pk_f16_f32 v58, v6, v7
	v_cvt_pk_f16_f32 v59, v8, v9
	v_exp_f32_e32 v11, v11
	v_pk_fma_f32 v[12:13], v[12:13], v[84:85], v[48:49] op_sel_hi:[1,0,0] neg_lo:[0,0,1] neg_hi:[0,0,1]
	v_exp_f32_e32 v12, v12
	v_mfma_f32_32x32x16_f16 v[18:33], v[56:59], v[40:43], 0
	v_exp_f32_e32 v13, v13
	v_pk_fma_f32 v[14:15], v[14:15], v[84:85], v[48:49] op_sel_hi:[1,0,0] neg_lo:[0,0,1] neg_hi:[0,0,1]
	v_exp_f32_e32 v14, v14
	v_exp_f32_e32 v15, v15
	v_pk_fma_f32 v[16:17], v[16:17], v[84:85], v[48:49] op_sel_hi:[1,0,0] neg_lo:[0,0,1] neg_hi:[0,0,1]
	v_exp_f32_e32 v16, v16
	v_exp_f32_e32 v17, v17
	v_cvt_pk_f16_f32 v60, v10, v11
	v_cvt_pk_f16_f32 v61, v12, v13
	v_cvt_pk_f16_f32 v62, v14, v15
	v_cvt_pk_f16_f32 v63, v16, v17
	s_nop 1
	v_mfma_f32_32x32x16_f16 v[18:33], v[60:63], v[44:47], v[18:33]
	s_nop 11
	v_log_f32_e32 v18, v18
	v_log_f32_e32 v19, v19
	v_log_f32_e32 v20, v20
	v_log_f32_e32 v21, v21
	v_log_f32_e32 v22, v22
	v_log_f32_e32 v23, v23
	v_pk_fma_f32 v[64:65], v[18:19], v[84:85], v[64:65] op_sel:[0,1,0] op_sel_hi:[1,1,1]
	buffer_store_dword v64, v36, s[8:11], 0 offen
	buffer_store_dword v65, v36, s[8:11], s24 offen
	v_log_f32_e32 v24, v24
	v_log_f32_e32 v25, v25
	v_pk_fma_f32 v[66:67], v[20:21], v[84:85], v[66:67] op_sel:[0,1,0] op_sel_hi:[1,1,1]
	buffer_store_dword v66, v36, s[8:11], s25 offen
	buffer_store_dword v67, v36, s[8:11], s26 offen
	v_log_f32_e32 v26, v26
	v_log_f32_e32 v27, v27
	v_pk_fma_f32 v[68:69], v[22:23], v[84:85], v[68:69] op_sel:[0,1,0] op_sel_hi:[1,1,1]
	buffer_store_dword v68, v36, s[8:11], s27 offen
	buffer_store_dword v69, v36, s[8:11], s28 offen
	v_log_f32_e32 v28, v28
	v_log_f32_e32 v29, v29
	v_pk_fma_f32 v[70:71], v[24:25], v[84:85], v[70:71] op_sel:[0,1,0] op_sel_hi:[1,1,1]
	buffer_store_dword v70, v36, s[8:11], s29 offen
	buffer_store_dword v71, v36, s[8:11], s30 offen
	v_log_f32_e32 v30, v30
	v_log_f32_e32 v31, v31
	v_pk_fma_f32 v[72:73], v[26:27], v[84:85], v[72:73] op_sel:[0,1,0] op_sel_hi:[1,1,1]
	buffer_store_dword v72, v36, s[8:11], s31 offen
	buffer_store_dword v73, v36, s[8:11], s32 offen
	v_log_f32_e32 v32, v32
	v_log_f32_e32 v33, v33
	v_pk_fma_f32 v[74:75], v[28:29], v[84:85], v[74:75] op_sel:[0,1,0] op_sel_hi:[1,1,1]
	buffer_store_dword v74, v36, s[8:11], s33 offen
	buffer_store_dword v75, v36, s[8:11], s34 offen
	v_pk_fma_f32 v[76:77], v[30:31], v[84:85], v[76:77] op_sel:[0,1,0] op_sel_hi:[1,1,1]
	buffer_store_dword v76, v36, s[8:11], s35 offen
	buffer_store_dword v77, v36, s[8:11], s36 offen
	v_pk_fma_f32 v[78:79], v[32:33], v[84:85], v[78:79] op_sel:[0,1,0] op_sel_hi:[1,1,1]
	buffer_store_dword v78, v36, s[8:11], s37 offen
	buffer_store_dword v79, v36, s[8:11], s38 offen
	s_endpgm

	.amdhsa_kernel _Z16sum_layer_kernelPKfS0_Pf
		.amdhsa_group_segment_fixed_size 18432
		.amdhsa_private_segment_fixed_size 0
		.amdhsa_kernarg_size 24
		.amdhsa_user_sgpr_count 2
		.amdhsa_user_sgpr_dispatch_ptr 0
		.amdhsa_user_sgpr_queue_ptr 0
		.amdhsa_user_sgpr_kernarg_segment_ptr 1
		.amdhsa_user_sgpr_dispatch_id 0
		.amdhsa_user_sgpr_kernarg_preload_length 0
		.amdhsa_user_sgpr_kernarg_preload_offset 0
		.amdhsa_user_sgpr_private_segment_size 0
		.amdhsa_uses_dynamic_stack 0
		.amdhsa_enable_private_segment 0
		.amdhsa_system_sgpr_workgroup_id_x 1
		.amdhsa_system_sgpr_workgroup_id_y 0
		.amdhsa_system_sgpr_workgroup_id_z 0
		.amdhsa_system_sgpr_workgroup_info 0
		.amdhsa_system_vgpr_workitem_id 0
		.amdhsa_next_free_vgpr 88
		.amdhsa_next_free_sgpr 41
		.amdhsa_accum_offset 88
		.amdhsa_reserve_vcc 1
		.amdhsa_float_round_mode_32 0
		.amdhsa_float_round_mode_16_64 0
		.amdhsa_float_denorm_mode_32 3
		.amdhsa_float_denorm_mode_16_64 3
		.amdhsa_dx10_clamp 1
		.amdhsa_ieee_mode 1
		.amdhsa_fp16_overflow 0
		.amdhsa_tg_split 0
		.amdhsa_exception_fp_ieee_invalid_op 0
		.amdhsa_exception_fp_denorm_src 0
		.amdhsa_exception_fp_ieee_div_zero 0
		.amdhsa_exception_fp_ieee_overflow 0
		.amdhsa_exception_fp_ieee_underflow 0
		.amdhsa_exception_fp_ieee_inexact 0
		.amdhsa_exception_int_div_zero 0
	.end_amdhsa_kernel

amdhsa.kernels:
  - .agpr_count:     0
    .args:
      - .address_space:  global
        .offset:         0
        .size:           8
        .value_kind:     global_buffer
      - .address_space:  global
        .offset:         8
        .size:           8
        .value_kind:     global_buffer
      - .address_space:  global
        .offset:         16
        .size:           8
        .value_kind:     global_buffer
    .group_segment_fixed_size: 18432
    .kernarg_segment_align: 8
    .kernarg_segment_size: 24
    .language:       OpenCL C
    .language_version:
      - 2
      - 0
    .max_flat_workgroup_size: 256
    .name:           _Z16sum_layer_kernelPKfS0_Pf
    .private_segment_fixed_size: 0
    .sgpr_count:     47
    .sgpr_spill_count: 0
    .symbol:         _Z16sum_layer_kernelPKfS0_Pf.kd
    .uniform_work_group_size: 1
    .uses_dynamic_stack: false
    .vgpr_count:     88
    .vgpr_spill_count: 0
    .wavefront_size: 64
